# speedup vs baseline: 1.0104x; 1.0104x over previous
.LBB1_4:
	v_add_u32_e32 v182, s19, v191
	v_add_u32_e32 v238, s19, v192
	ds_read_b128 v[178:181], v182 offset:32768
	ds_read_b128 v[194:197], v182 offset:34816
	ds_read_b128 v[198:201], v182 offset:36864
	ds_read_b128 v[202:205], v182 offset:38912
	ds_read_b128 v[206:209], v238
	ds_read_b128 v[210:213], v238 offset:2048
	ds_read_b128 v[214:217], v238 offset:4096
	ds_read_b128 v[218:221], v238 offset:6144
	ds_read_b128 v[222:225], v238 offset:8192
	ds_read_b128 v[226:229], v238 offset:10240
	ds_read_b128 v[230:233], v238 offset:12288
	ds_read_b128 v[234:237], v238 offset:14336
	s_min_u32 s21, s20, 29
	s_xor_b32 s19, s19, 0x10000
	v_add_u32_e32 v239, s19, v189
	s_waitcnt vmcnt(11)
	v_cvt_pk_bf16_f32 v13, v12, v13
	v_cvt_pk_bf16_f32 v12, v10, v11
	s_waitcnt vmcnt(10)
	v_cvt_pk_bf16_f32 v11, v20, v21
	v_cvt_pk_bf16_f32 v10, v18, v19
	ds_write2st64_b64 v239, v[12:13], v[10:11] offset1:8
	s_waitcnt vmcnt(9)
	v_cvt_pk_bf16_f32 v11, v24, v25
	v_cvt_pk_bf16_f32 v10, v22, v23
	s_waitcnt vmcnt(8)
	v_cvt_pk_bf16_f32 v13, v32, v33
	v_cvt_pk_bf16_f32 v12, v30, v31
	ds_write2st64_b64 v239, v[10:11], v[12:13] offset0:16 offset1:24
	s_waitcnt vmcnt(7)
	v_cvt_pk_bf16_f32 v11, v36, v37
	v_cvt_pk_bf16_f32 v10, v34, v35
	s_waitcnt vmcnt(6)
	v_cvt_pk_bf16_f32 v13, v40, v41
	v_cvt_pk_bf16_f32 v12, v38, v39
	ds_write2st64_b64 v239, v[10:11], v[12:13] offset0:32 offset1:40
	s_waitcnt vmcnt(5)
	v_cvt_pk_bf16_f32 v11, v44, v45
	v_cvt_pk_bf16_f32 v10, v42, v43
	s_waitcnt vmcnt(4)
	v_cvt_pk_bf16_f32 v13, v48, v49
	v_cvt_pk_bf16_f32 v12, v46, v47
	ds_write2st64_b64 v239, v[10:11], v[12:13] offset0:48 offset1:56
	s_waitcnt lgkmcnt(0)
	s_add_i32 s21, s21, 2
	s_barrier
	s_waitcnt lgkmcnt(11)
	v_mfma_f32_16x16x32_bf16 v[174:177], v[178:181], v[206:209], v[174:177]
	s_lshl_b32 s22, s21, 1
	s_and_b32 s22, s22, 0x60
	s_add_i32 s22, s22, s12
	s_lshl_b32 s22, s22, 6
	v_mfma_f32_16x16x32_bf16 v[170:173], v[194:197], v[206:209], v[170:173]
	s_and_b32 s22, s22, 0x3f00
	s_or_b32 s22, s22, s13
	s_lshl_b32 s23, s21, 23
	s_lshl_b32 s22, s22, 9
	v_mfma_f32_16x16x32_bf16 v[158:161], v[198:201], v[206:209], v[158:161]
	s_and_b32 s23, s23, 0x7000000
	s_or_b32 s22, s22, s23
	s_lshl_b32 s23, s21, 8
	s_and_b32 s23, s23, 0x100
	s_or_b32 s22, s22, s23
	s_or_b32 s23, s22, 0x4000
	buffer_load_dwordx4 v[10:13], v1, s[4:7], s22 offen sc0 nt
	v_mfma_f32_16x16x32_bf16 v[142:145], v[202:205], v[206:209], v[142:145]
	s_waitcnt lgkmcnt(10)
	v_mfma_f32_16x16x32_bf16 v[166:169], v[178:181], v[210:213], v[166:169]
	v_mfma_f32_16x16x32_bf16 v[162:165], v[194:197], v[210:213], v[162:165]
	v_mfma_f32_16x16x32_bf16 v[146:149], v[198:201], v[210:213], v[146:149]
	buffer_load_dwordx4 v[18:21], v1, s[4:7], s23 offen sc0 nt
	s_or_b32 s23, s22, 0x8000
	v_mfma_f32_16x16x32_bf16 v[122:125], v[202:205], v[210:213], v[122:125]
	s_waitcnt lgkmcnt(9)
	v_mfma_f32_16x16x32_bf16 v[154:157], v[178:181], v[214:217], v[154:157]
	v_mfma_f32_16x16x32_bf16 v[150:153], v[194:197], v[214:217], v[150:153]
	v_mfma_f32_16x16x32_bf16 v[130:133], v[198:201], v[214:217], v[130:133]
	buffer_load_dwordx4 v[22:25], v1, s[4:7], s23 offen sc0 nt
	s_or_b32 s23, s22, 0xc000
	v_mfma_f32_16x16x32_bf16 v[106:109], v[202:205], v[214:217], v[106:109]
	s_waitcnt lgkmcnt(8)
	v_mfma_f32_16x16x32_bf16 v[138:141], v[178:181], v[218:221], v[138:141]
	v_mfma_f32_16x16x32_bf16 v[134:137], v[194:197], v[218:221], v[134:137]
	v_mfma_f32_16x16x32_bf16 v[114:117], v[198:201], v[218:221], v[114:117]
	buffer_load_dwordx4 v[30:33], v1, s[4:7], s23 offen sc0 nt
	s_or_b32 s23, s22, 0x10000
	v_mfma_f32_16x16x32_bf16 v[90:93], v[202:205], v[218:221], v[90:93]
	s_waitcnt lgkmcnt(7)
	v_mfma_f32_16x16x32_bf16 v[126:129], v[178:181], v[222:225], v[126:129]
	v_mfma_f32_16x16x32_bf16 v[118:121], v[194:197], v[222:225], v[118:121]
	v_mfma_f32_16x16x32_bf16 v[98:101], v[198:201], v[222:225], v[98:101]
	buffer_load_dwordx4 v[34:37], v1, s[4:7], s23 offen sc0 nt
	s_or_b32 s23, s22, 0x14000
	v_mfma_f32_16x16x32_bf16 v[74:77], v[202:205], v[222:225], v[74:77]
	s_waitcnt lgkmcnt(6)
	v_mfma_f32_16x16x32_bf16 v[110:113], v[178:181], v[226:229], v[110:113]
	v_mfma_f32_16x16x32_bf16 v[102:105], v[194:197], v[226:229], v[102:105]
	v_mfma_f32_16x16x32_bf16 v[82:85], v[198:201], v[226:229], v[82:85]
	buffer_load_dwordx4 v[38:41], v1, s[4:7], s23 offen sc0 nt
	s_or_b32 s23, s22, 0x18000
	s_or_b32 s22, s22, 0x1c000
	v_mfma_f32_16x16x32_bf16 v[62:65], v[202:205], v[226:229], v[62:65]
	s_waitcnt lgkmcnt(5)
	v_mfma_f32_16x16x32_bf16 v[94:97], v[178:181], v[230:233], v[94:97]
	v_mfma_f32_16x16x32_bf16 v[86:89], v[194:197], v[230:233], v[86:89]
	v_mfma_f32_16x16x32_bf16 v[70:73], v[198:201], v[230:233], v[70:73]
	buffer_load_dwordx4 v[42:45], v1, s[4:7], s23 offen sc0 nt
	v_mfma_f32_16x16x32_bf16 v[54:57], v[202:205], v[230:233], v[54:57]
	s_waitcnt lgkmcnt(4)
	v_mfma_f32_16x16x32_bf16 v[78:81], v[178:181], v[234:237], v[78:81]
	v_mfma_f32_16x16x32_bf16 v[66:69], v[194:197], v[234:237], v[66:69]
	v_mfma_f32_16x16x32_bf16 v[58:61], v[198:201], v[234:237], v[58:61]
	buffer_load_dwordx4 v[46:49], v1, s[4:7], s22 offen sc0 nt
	v_mfma_f32_16x16x32_bf16 v[50:53], v[202:205], v[234:237], v[50:53]
	s_waitcnt lgkmcnt(0)
	s_barrier
	ds_read_b128 v[178:181], v182 offset:33792
	ds_read_b128 v[194:197], v182 offset:35840
	ds_read_b128 v[198:201], v182 offset:37888
	ds_read_b128 v[202:205], v182 offset:39936
	ds_read_b128 v[206:209], v238 offset:1024
	ds_read_b128 v[210:213], v238 offset:3072
	ds_read_b128 v[214:217], v238 offset:5120
	ds_read_b128 v[218:221], v238 offset:7168
	ds_read_b128 v[222:225], v238 offset:9216
	ds_read_b128 v[226:229], v238 offset:11264
	ds_read_b128 v[230:233], v238 offset:13312
	ds_read_b128 v[234:237], v238 offset:15360
	v_add_u32_e32 v182, s19, v190
	s_waitcnt vmcnt(11)
	ds_write_b128 v182, v[2:5] offset:32768
	s_waitcnt vmcnt(10)
	ds_write_b128 v182, v[6:9] offset:40960
	s_waitcnt vmcnt(9)
	ds_write_b128 v182, v[14:17] offset:49152
	s_waitcnt vmcnt(8)
	ds_write_b128 v182, v[26:29] offset:57344
	s_waitcnt lgkmcnt(0)
	s_barrier
	s_waitcnt lgkmcnt(11)
	v_mfma_f32_16x16x32_bf16 v[174:177], v[178:181], v[206:209], v[174:177]
	s_lshl_b32 s21, s21, 7
	s_and_b32 s21, s21, 0x780
	s_or_b32 s21, s21, s14
	s_or_b32 s22, s21, 0x20000
	v_mfma_f32_16x16x32_bf16 v[170:173], v[194:197], v[206:209], v[170:173]
	v_mfma_f32_16x16x32_bf16 v[158:161], v[198:201], v[206:209], v[158:161]
	v_mfma_f32_16x16x32_bf16 v[142:145], v[202:205], v[206:209], v[142:145]
	s_waitcnt lgkmcnt(10)
	v_mfma_f32_16x16x32_bf16 v[166:169], v[178:181], v[210:213], v[166:169]
	v_mfma_f32_16x16x32_bf16 v[162:165], v[194:197], v[210:213], v[162:165]
	buffer_load_dwordx4 v[2:5], v188, s[0:3], s21 offen sc1
	v_mfma_f32_16x16x32_bf16 v[146:149], v[198:201], v[210:213], v[146:149]
	v_mfma_f32_16x16x32_bf16 v[122:125], v[202:205], v[210:213], v[122:125]
	s_waitcnt lgkmcnt(9)
	v_mfma_f32_16x16x32_bf16 v[154:157], v[178:181], v[214:217], v[154:157]
	v_mfma_f32_16x16x32_bf16 v[150:153], v[194:197], v[214:217], v[150:153]
	v_mfma_f32_16x16x32_bf16 v[130:133], v[198:201], v[214:217], v[130:133]
	v_mfma_f32_16x16x32_bf16 v[106:109], v[202:205], v[214:217], v[106:109]
	s_waitcnt lgkmcnt(8)
	v_mfma_f32_16x16x32_bf16 v[138:141], v[178:181], v[218:221], v[138:141]
	v_mfma_f32_16x16x32_bf16 v[134:137], v[194:197], v[218:221], v[134:137]
	buffer_load_dwordx4 v[6:9], v188, s[0:3], s22 offen sc1
	s_or_b32 s22, s21, 0x40000
	s_or_b32 s21, s21, 0x60000
	v_mfma_f32_16x16x32_bf16 v[114:117], v[198:201], v[218:221], v[114:117]
	v_mfma_f32_16x16x32_bf16 v[90:93], v[202:205], v[218:221], v[90:93]
	s_waitcnt lgkmcnt(7)
	v_mfma_f32_16x16x32_bf16 v[126:129], v[178:181], v[222:225], v[126:129]
	v_mfma_f32_16x16x32_bf16 v[118:121], v[194:197], v[222:225], v[118:121]
	v_mfma_f32_16x16x32_bf16 v[98:101], v[198:201], v[222:225], v[98:101]
	v_mfma_f32_16x16x32_bf16 v[74:77], v[202:205], v[222:225], v[74:77]
	s_waitcnt lgkmcnt(6)
	v_mfma_f32_16x16x32_bf16 v[110:113], v[178:181], v[226:229], v[110:113]
	v_mfma_f32_16x16x32_bf16 v[102:105], v[194:197], v[226:229], v[102:105]
	buffer_load_dwordx4 v[14:17], v188, s[0:3], s22 offen sc1
	v_mfma_f32_16x16x32_bf16 v[82:85], v[198:201], v[226:229], v[82:85]
	v_mfma_f32_16x16x32_bf16 v[62:65], v[202:205], v[226:229], v[62:65]
	s_waitcnt lgkmcnt(5)
	v_mfma_f32_16x16x32_bf16 v[94:97], v[178:181], v[230:233], v[94:97]
	v_mfma_f32_16x16x32_bf16 v[86:89], v[194:197], v[230:233], v[86:89]
	v_mfma_f32_16x16x32_bf16 v[70:73], v[198:201], v[230:233], v[70:73]
	v_mfma_f32_16x16x32_bf16 v[54:57], v[202:205], v[230:233], v[54:57]
	s_waitcnt lgkmcnt(4)
	v_mfma_f32_16x16x32_bf16 v[78:81], v[178:181], v[234:237], v[78:81]
	v_mfma_f32_16x16x32_bf16 v[66:69], v[194:197], v[234:237], v[66:69]
	buffer_load_dwordx4 v[26:29], v188, s[0:3], s21 offen sc1
	v_mfma_f32_16x16x32_bf16 v[58:61], v[198:201], v[234:237], v[58:61]
	v_mfma_f32_16x16x32_bf16 v[50:53], v[202:205], v[234:237], v[50:53]
	s_and_b32 s21, s20, 15
	s_cmp_lg_u32 s21, 15
	s_cbranch_scc1 .LBB1_3
	s_and_b32 s21, s18, 32
	s_add_i32 s21, s21, s12
	s_lshl_b32 s21, s21, 6
	s_and_b32 s21, s21, 0x3f00
	v_add_lshl_u32 v182, v193, s21, 9
	v_lshl_add_u64 v[206:207], v[184:185], 0, v[182:183]
	v_add_co_u32_e32 v208, vcc, s8, v206
	s_nop 1
	v_addc_co_u32_e32 v209, vcc, 0, v207, vcc
	v_add_co_u32_e32 v210, vcc, s15, v206
	s_nop 1
	v_addc_co_u32_e32 v211, vcc, 0, v207, vcc
	v_add_co_u32_e32 v212, vcc, s9, v206
	s_nop 1
	v_addc_co_u32_e32 v213, vcc, 0, v207, vcc
	v_add_co_u32_e32 v214, vcc, s16, v206
	s_nop 1
	v_addc_co_u32_e32 v215, vcc, 0, v207, vcc
	v_add_co_u32_e32 v216, vcc, s10, v206
	s_nop 1
	v_addc_co_u32_e32 v217, vcc, 0, v207, vcc
	v_add_co_u32_e32 v218, vcc, s17, v206
	s_nop 1
	v_addc_co_u32_e32 v219, vcc, 0, v207, vcc
	v_add_co_u32_e32 v220, vcc, s11, v206
	s_nop 1
	v_addc_co_u32_e32 v221, vcc, 0, v207, vcc
	global_store_dwordx4 v[206:207], v[174:177], off
	global_store_dwordx4 v[206:207], v[170:173], off offset:64
	global_store_dwordx4 v[206:207], v[158:161], off offset:128
	global_store_dwordx4 v[206:207], v[142:145], off offset:192
	global_store_dwordx4 v[208:209], v[166:169], off
	global_store_dwordx4 v[208:209], v[162:165], off offset:64
	global_store_dwordx4 v[208:209], v[146:149], off offset:128
	global_store_dwordx4 v[208:209], v[122:125], off offset:192
	global_store_dwordx4 v[210:211], v[154:157], off
	global_store_dwordx4 v[210:211], v[150:153], off offset:64
	global_store_dwordx4 v[210:211], v[130:133], off offset:128
	global_store_dwordx4 v[210:211], v[106:109], off offset:192
	global_store_dwordx4 v[212:213], v[138:141], off
	global_store_dwordx4 v[212:213], v[134:137], off offset:64
	global_store_dwordx4 v[212:213], v[114:117], off offset:128
	global_store_dwordx4 v[212:213], v[90:93], off offset:192
	global_store_dwordx4 v[214:215], v[126:129], off
	global_store_dwordx4 v[214:215], v[118:121], off offset:64
	global_store_dwordx4 v[214:215], v[98:101], off offset:128
	global_store_dwordx4 v[214:215], v[74:77], off offset:192
	global_store_dwordx4 v[216:217], v[110:113], off
	global_store_dwordx4 v[216:217], v[102:105], off offset:64
	global_store_dwordx4 v[216:217], v[82:85], off offset:128
	global_store_dwordx4 v[216:217], v[62:65], off offset:192
	global_store_dwordx4 v[218:219], v[94:97], off
	global_store_dwordx4 v[218:219], v[86:89], off offset:64
	global_store_dwordx4 v[218:219], v[70:73], off offset:128
	global_store_dwordx4 v[218:219], v[54:57], off offset:192
	global_store_dwordx4 v[220:221], v[78:81], off
	global_store_dwordx4 v[220:221], v[66:69], off offset:64
	global_store_dwordx4 v[220:221], v[58:61], off offset:128
	global_store_dwordx4 v[220:221], v[50:53], off offset:192
.Lpd_tail:
	s_waitcnt lgkmcnt(0)
	s_barrier
	s_add_i32 s20, s20, 1
	s_add_i32 s18, s18, 2
	v_add_u32_e32 v182, s19, v191
	v_add_u32_e32 v238, s19, v192
	ds_read_b128 v[178:181], v182 offset:32768
	ds_read_b128 v[194:197], v182 offset:34816
	ds_read_b128 v[198:201], v182 offset:36864
	ds_read_b128 v[202:205], v182 offset:38912
	ds_read_b128 v[206:209], v238
	ds_read_b128 v[210:213], v238 offset:2048
	ds_read_b128 v[214:217], v238 offset:4096
	ds_read_b128 v[218:221], v238 offset:6144
	ds_read_b128 v[222:225], v238 offset:8192
	ds_read_b128 v[226:229], v238 offset:10240
	ds_read_b128 v[230:233], v238 offset:12288
	ds_read_b128 v[234:237], v238 offset:14336
	s_min_u32 s21, s20, 29
	s_xor_b32 s19, s19, 0x10000
	v_add_u32_e32 v239, s19, v189
	s_waitcnt vmcnt(43)
	v_cvt_pk_bf16_f32 v13, v12, v13
	v_cvt_pk_bf16_f32 v12, v10, v11
	s_waitcnt vmcnt(42)
	v_cvt_pk_bf16_f32 v11, v20, v21
	v_cvt_pk_bf16_f32 v10, v18, v19
	ds_write2st64_b64 v239, v[12:13], v[10:11] offset1:8
	s_waitcnt vmcnt(41)
	v_cvt_pk_bf16_f32 v11, v24, v25
	v_cvt_pk_bf16_f32 v10, v22, v23
	s_waitcnt vmcnt(40)
	v_cvt_pk_bf16_f32 v13, v32, v33
	v_cvt_pk_bf16_f32 v12, v30, v31
	ds_write2st64_b64 v239, v[10:11], v[12:13] offset0:16 offset1:24
	s_waitcnt vmcnt(39)
	v_cvt_pk_bf16_f32 v11, v36, v37
	v_cvt_pk_bf16_f32 v10, v34, v35
	s_waitcnt vmcnt(38)
	v_cvt_pk_bf16_f32 v13, v40, v41
	v_cvt_pk_bf16_f32 v12, v38, v39
	ds_write2st64_b64 v239, v[10:11], v[12:13] offset0:32 offset1:40
	s_waitcnt vmcnt(37)
	v_cvt_pk_bf16_f32 v11, v44, v45
	v_cvt_pk_bf16_f32 v10, v42, v43
	s_waitcnt vmcnt(36)
	v_cvt_pk_bf16_f32 v13, v48, v49
	v_cvt_pk_bf16_f32 v12, v46, v47
	ds_write2st64_b64 v239, v[10:11], v[12:13] offset0:48 offset1:56
	s_waitcnt lgkmcnt(0)
	s_add_i32 s21, s21, 2
	s_barrier
	s_waitcnt lgkmcnt(11)
	v_mfma_f32_16x16x32_bf16 v[174:177], v[178:181], v[206:209], v[240:243]
	s_lshl_b32 s22, s21, 1
	s_and_b32 s22, s22, 0x60
	s_add_i32 s22, s22, s12
	s_lshl_b32 s22, s22, 6
	v_mfma_f32_16x16x32_bf16 v[170:173], v[194:197], v[206:209], v[244:247]
	s_and_b32 s22, s22, 0x3f00
	s_or_b32 s22, s22, s13
	s_lshl_b32 s23, s21, 23
	s_lshl_b32 s22, s22, 9
	v_mfma_f32_16x16x32_bf16 v[158:161], v[198:201], v[206:209], v[248:251]
	s_and_b32 s23, s23, 0x7000000
	s_or_b32 s22, s22, s23
	s_lshl_b32 s23, s21, 8
	s_and_b32 s23, s23, 0x100
	s_or_b32 s22, s22, s23
	s_or_b32 s23, s22, 0x4000
	buffer_load_dwordx4 v[10:13], v1, s[4:7], s22 offen sc0 nt
	v_mfma_f32_16x16x32_bf16 v[142:145], v[202:205], v[206:209], v[252:255]
	s_waitcnt lgkmcnt(10)
	v_mfma_f32_16x16x32_bf16 v[166:169], v[178:181], v[210:213], v[240:243]
	v_mfma_f32_16x16x32_bf16 v[162:165], v[194:197], v[210:213], v[244:247]
	v_mfma_f32_16x16x32_bf16 v[146:149], v[198:201], v[210:213], v[248:251]
	buffer_load_dwordx4 v[18:21], v1, s[4:7], s23 offen sc0 nt
	s_or_b32 s23, s22, 0x8000
	v_mfma_f32_16x16x32_bf16 v[122:125], v[202:205], v[210:213], v[252:255]
	s_waitcnt lgkmcnt(9)
	v_mfma_f32_16x16x32_bf16 v[154:157], v[178:181], v[214:217], v[240:243]
	v_mfma_f32_16x16x32_bf16 v[150:153], v[194:197], v[214:217], v[244:247]
	v_mfma_f32_16x16x32_bf16 v[130:133], v[198:201], v[214:217], v[248:251]
	buffer_load_dwordx4 v[22:25], v1, s[4:7], s23 offen sc0 nt
	s_or_b32 s23, s22, 0xc000
	v_mfma_f32_16x16x32_bf16 v[106:109], v[202:205], v[214:217], v[252:255]
	s_waitcnt lgkmcnt(8)
	v_mfma_f32_16x16x32_bf16 v[138:141], v[178:181], v[218:221], v[240:243]
	v_mfma_f32_16x16x32_bf16 v[134:137], v[194:197], v[218:221], v[244:247]
	v_mfma_f32_16x16x32_bf16 v[114:117], v[198:201], v[218:221], v[248:251]
	buffer_load_dwordx4 v[30:33], v1, s[4:7], s23 offen sc0 nt
	s_or_b32 s23, s22, 0x10000
	v_mfma_f32_16x16x32_bf16 v[90:93], v[202:205], v[218:221], v[252:255]
	s_waitcnt lgkmcnt(7)
	v_mfma_f32_16x16x32_bf16 v[126:129], v[178:181], v[222:225], v[240:243]
	v_mfma_f32_16x16x32_bf16 v[118:121], v[194:197], v[222:225], v[244:247]
	v_mfma_f32_16x16x32_bf16 v[98:101], v[198:201], v[222:225], v[248:251]
	buffer_load_dwordx4 v[34:37], v1, s[4:7], s23 offen sc0 nt
	s_or_b32 s23, s22, 0x14000
	v_mfma_f32_16x16x32_bf16 v[74:77], v[202:205], v[222:225], v[252:255]
	s_waitcnt lgkmcnt(6)
	v_mfma_f32_16x16x32_bf16 v[110:113], v[178:181], v[226:229], v[240:243]
	v_mfma_f32_16x16x32_bf16 v[102:105], v[194:197], v[226:229], v[244:247]
	v_mfma_f32_16x16x32_bf16 v[82:85], v[198:201], v[226:229], v[248:251]
	buffer_load_dwordx4 v[38:41], v1, s[4:7], s23 offen sc0 nt
	s_or_b32 s23, s22, 0x18000
	s_or_b32 s22, s22, 0x1c000
	v_mfma_f32_16x16x32_bf16 v[62:65], v[202:205], v[226:229], v[252:255]
	s_waitcnt lgkmcnt(5)
	v_mfma_f32_16x16x32_bf16 v[94:97], v[178:181], v[230:233], v[240:243]
	v_mfma_f32_16x16x32_bf16 v[86:89], v[194:197], v[230:233], v[244:247]
	v_mfma_f32_16x16x32_bf16 v[70:73], v[198:201], v[230:233], v[248:251]
	buffer_load_dwordx4 v[42:45], v1, s[4:7], s23 offen sc0 nt
	v_mfma_f32_16x16x32_bf16 v[54:57], v[202:205], v[230:233], v[252:255]
	s_waitcnt lgkmcnt(4)
	v_mfma_f32_16x16x32_bf16 v[78:81], v[178:181], v[234:237], v[240:243]
	v_mfma_f32_16x16x32_bf16 v[66:69], v[194:197], v[234:237], v[244:247]
	v_mfma_f32_16x16x32_bf16 v[58:61], v[198:201], v[234:237], v[248:251]
	buffer_load_dwordx4 v[46:49], v1, s[4:7], s22 offen sc0 nt
	v_mfma_f32_16x16x32_bf16 v[50:53], v[202:205], v[234:237], v[252:255]
	s_waitcnt lgkmcnt(0)
	s_barrier
	ds_read_b128 v[178:181], v182 offset:33792
	ds_read_b128 v[194:197], v182 offset:35840
	ds_read_b128 v[198:201], v182 offset:37888
	ds_read_b128 v[202:205], v182 offset:39936
	ds_read_b128 v[206:209], v238 offset:1024
	ds_read_b128 v[210:213], v238 offset:3072
	ds_read_b128 v[214:217], v238 offset:5120
	ds_read_b128 v[218:221], v238 offset:7168
	ds_read_b128 v[222:225], v238 offset:9216
	ds_read_b128 v[226:229], v238 offset:11264
	ds_read_b128 v[230:233], v238 offset:13312
	ds_read_b128 v[234:237], v238 offset:15360
	v_add_u32_e32 v182, s19, v190
	s_waitcnt vmcnt(43)
	ds_write_b128 v182, v[2:5] offset:32768
	s_waitcnt vmcnt(42)
	ds_write_b128 v182, v[6:9] offset:40960
	s_waitcnt vmcnt(41)
	ds_write_b128 v182, v[14:17] offset:49152
	s_waitcnt vmcnt(40)
	ds_write_b128 v182, v[26:29] offset:57344
	s_waitcnt lgkmcnt(0)
	s_barrier
	s_waitcnt lgkmcnt(11)
	v_mfma_f32_16x16x32_bf16 v[174:177], v[178:181], v[206:209], v[174:177]
	s_lshl_b32 s21, s21, 7
	s_and_b32 s21, s21, 0x780
	s_or_b32 s21, s21, s14
	s_or_b32 s22, s21, 0x20000
	v_mfma_f32_16x16x32_bf16 v[170:173], v[194:197], v[206:209], v[170:173]
	v_mfma_f32_16x16x32_bf16 v[158:161], v[198:201], v[206:209], v[158:161]
	v_mfma_f32_16x16x32_bf16 v[142:145], v[202:205], v[206:209], v[142:145]
	s_waitcnt lgkmcnt(10)
	v_mfma_f32_16x16x32_bf16 v[166:169], v[178:181], v[210:213], v[166:169]
	v_mfma_f32_16x16x32_bf16 v[162:165], v[194:197], v[210:213], v[162:165]
	buffer_load_dwordx4 v[2:5], v188, s[0:3], s21 offen sc1
	v_mfma_f32_16x16x32_bf16 v[146:149], v[198:201], v[210:213], v[146:149]
	v_mfma_f32_16x16x32_bf16 v[122:125], v[202:205], v[210:213], v[122:125]
	s_waitcnt lgkmcnt(9)
	v_mfma_f32_16x16x32_bf16 v[154:157], v[178:181], v[214:217], v[154:157]
	v_mfma_f32_16x16x32_bf16 v[150:153], v[194:197], v[214:217], v[150:153]
	v_mfma_f32_16x16x32_bf16 v[130:133], v[198:201], v[214:217], v[130:133]
	v_mfma_f32_16x16x32_bf16 v[106:109], v[202:205], v[214:217], v[106:109]
	s_waitcnt lgkmcnt(8)
	v_mfma_f32_16x16x32_bf16 v[138:141], v[178:181], v[218:221], v[138:141]
	v_mfma_f32_16x16x32_bf16 v[134:137], v[194:197], v[218:221], v[134:137]
	buffer_load_dwordx4 v[6:9], v188, s[0:3], s22 offen sc1
	s_or_b32 s22, s21, 0x40000
	s_or_b32 s21, s21, 0x60000
	v_mfma_f32_16x16x32_bf16 v[114:117], v[198:201], v[218:221], v[114:117]
	v_mfma_f32_16x16x32_bf16 v[90:93], v[202:205], v[218:221], v[90:93]
	s_waitcnt lgkmcnt(7)
	v_mfma_f32_16x16x32_bf16 v[126:129], v[178:181], v[222:225], v[126:129]
	v_mfma_f32_16x16x32_bf16 v[118:121], v[194:197], v[222:225], v[118:121]
	v_mfma_f32_16x16x32_bf16 v[98:101], v[198:201], v[222:225], v[98:101]
	v_mfma_f32_16x16x32_bf16 v[74:77], v[202:205], v[222:225], v[74:77]
	s_waitcnt lgkmcnt(6)
	v_mfma_f32_16x16x32_bf16 v[110:113], v[178:181], v[226:229], v[110:113]
	v_mfma_f32_16x16x32_bf16 v[102:105], v[194:197], v[226:229], v[102:105]
	buffer_load_dwordx4 v[14:17], v188, s[0:3], s22 offen sc1
	v_mfma_f32_16x16x32_bf16 v[82:85], v[198:201], v[226:229], v[82:85]
	v_mfma_f32_16x16x32_bf16 v[62:65], v[202:205], v[226:229], v[62:65]
	s_waitcnt lgkmcnt(5)
	v_mfma_f32_16x16x32_bf16 v[94:97], v[178:181], v[230:233], v[94:97]
	v_mfma_f32_16x16x32_bf16 v[86:89], v[194:197], v[230:233], v[86:89]
	v_mfma_f32_16x16x32_bf16 v[70:73], v[198:201], v[230:233], v[70:73]
	v_mfma_f32_16x16x32_bf16 v[54:57], v[202:205], v[230:233], v[54:57]
	s_waitcnt lgkmcnt(4)
	v_mfma_f32_16x16x32_bf16 v[78:81], v[178:181], v[234:237], v[78:81]
	v_mfma_f32_16x16x32_bf16 v[66:69], v[194:197], v[234:237], v[66:69]
	buffer_load_dwordx4 v[26:29], v188, s[0:3], s21 offen sc1
	v_mfma_f32_16x16x32_bf16 v[58:61], v[198:201], v[234:237], v[58:61]
	v_mfma_f32_16x16x32_bf16 v[50:53], v[202:205], v[234:237], v[50:53]
	s_branch .LBB1_3
.Lt30:
	v_add_u32_e32 v182, s19, v191
	v_add_u32_e32 v238, s19, v192
	ds_read_b128 v[178:181], v182 offset:32768
	ds_read_b128 v[194:197], v182 offset:34816
	ds_read_b128 v[198:201], v182 offset:36864
	ds_read_b128 v[202:205], v182 offset:38912
	ds_read_b128 v[206:209], v238
	ds_read_b128 v[210:213], v238 offset:2048
	ds_read_b128 v[214:217], v238 offset:4096
	ds_read_b128 v[218:221], v238 offset:6144
	ds_read_b128 v[222:225], v238 offset:8192
	ds_read_b128 v[226:229], v238 offset:10240
	ds_read_b128 v[230:233], v238 offset:12288
	ds_read_b128 v[234:237], v238 offset:14336
	s_min_u32 s21, s20, 29
	s_xor_b32 s19, s19, 0x10000
	v_add_u32_e32 v239, s19, v189
	s_waitcnt vmcnt(11)
	v_cvt_pk_bf16_f32 v13, v12, v13
	v_cvt_pk_bf16_f32 v12, v10, v11
	s_waitcnt vmcnt(10)
	v_cvt_pk_bf16_f32 v11, v20, v21
	v_cvt_pk_bf16_f32 v10, v18, v19
	ds_write2st64_b64 v239, v[12:13], v[10:11] offset1:8
	s_waitcnt vmcnt(9)
	v_cvt_pk_bf16_f32 v11, v24, v25
	v_cvt_pk_bf16_f32 v10, v22, v23
	s_waitcnt vmcnt(8)
	v_cvt_pk_bf16_f32 v13, v32, v33
	v_cvt_pk_bf16_f32 v12, v30, v31
	ds_write2st64_b64 v239, v[10:11], v[12:13] offset0:16 offset1:24
	s_waitcnt vmcnt(7)
	v_cvt_pk_bf16_f32 v11, v36, v37
	v_cvt_pk_bf16_f32 v10, v34, v35
	s_waitcnt vmcnt(6)
	v_cvt_pk_bf16_f32 v13, v40, v41
	v_cvt_pk_bf16_f32 v12, v38, v39
	ds_write2st64_b64 v239, v[10:11], v[12:13] offset0:32 offset1:40
	s_waitcnt vmcnt(5)
	v_cvt_pk_bf16_f32 v11, v44, v45
	v_cvt_pk_bf16_f32 v10, v42, v43
	s_waitcnt vmcnt(4)
	v_cvt_pk_bf16_f32 v13, v48, v49
	v_cvt_pk_bf16_f32 v12, v46, v47
	ds_write2st64_b64 v239, v[10:11], v[12:13] offset0:48 offset1:56
	s_waitcnt lgkmcnt(0)
	s_add_i32 s21, s21, 2
	s_barrier
	s_waitcnt lgkmcnt(11)
	v_mfma_f32_16x16x32_bf16 v[174:177], v[178:181], v[206:209], v[174:177]
	s_lshl_b32 s22, s21, 1
	s_and_b32 s22, s22, 0x60
	s_add_i32 s22, s22, s12
	s_lshl_b32 s22, s22, 6
	v_mfma_f32_16x16x32_bf16 v[170:173], v[194:197], v[206:209], v[170:173]
	s_and_b32 s22, s22, 0x3f00
	s_or_b32 s22, s22, s13
	s_lshl_b32 s23, s21, 23
	s_lshl_b32 s22, s22, 9
	v_mfma_f32_16x16x32_bf16 v[158:161], v[198:201], v[206:209], v[158:161]
	s_and_b32 s23, s23, 0x7000000
	s_or_b32 s22, s22, s23
	s_lshl_b32 s23, s21, 8
	s_and_b32 s23, s23, 0x100
	s_or_b32 s22, s22, s23
	s_or_b32 s23, s22, 0x4000
	v_mfma_f32_16x16x32_bf16 v[142:145], v[202:205], v[206:209], v[142:145]
	s_waitcnt lgkmcnt(10)
	v_mfma_f32_16x16x32_bf16 v[166:169], v[178:181], v[210:213], v[166:169]
	v_mfma_f32_16x16x32_bf16 v[162:165], v[194:197], v[210:213], v[162:165]
	v_mfma_f32_16x16x32_bf16 v[146:149], v[198:201], v[210:213], v[146:149]
	s_or_b32 s23, s22, 0x8000
	v_mfma_f32_16x16x32_bf16 v[122:125], v[202:205], v[210:213], v[122:125]
	s_waitcnt lgkmcnt(9)
	v_mfma_f32_16x16x32_bf16 v[154:157], v[178:181], v[214:217], v[154:157]
	v_mfma_f32_16x16x32_bf16 v[150:153], v[194:197], v[214:217], v[150:153]
	v_mfma_f32_16x16x32_bf16 v[130:133], v[198:201], v[214:217], v[130:133]
	s_or_b32 s23, s22, 0xc000
	v_mfma_f32_16x16x32_bf16 v[106:109], v[202:205], v[214:217], v[106:109]
	s_waitcnt lgkmcnt(8)
	v_mfma_f32_16x16x32_bf16 v[138:141], v[178:181], v[218:221], v[138:141]
	v_mfma_f32_16x16x32_bf16 v[134:137], v[194:197], v[218:221], v[134:137]
	v_mfma_f32_16x16x32_bf16 v[114:117], v[198:201], v[218:221], v[114:117]
	s_or_b32 s23, s22, 0x10000
	v_mfma_f32_16x16x32_bf16 v[90:93], v[202:205], v[218:221], v[90:93]
	s_waitcnt lgkmcnt(7)
	v_mfma_f32_16x16x32_bf16 v[126:129], v[178:181], v[222:225], v[126:129]
	v_mfma_f32_16x16x32_bf16 v[118:121], v[194:197], v[222:225], v[118:121]
	v_mfma_f32_16x16x32_bf16 v[98:101], v[198:201], v[222:225], v[98:101]
	s_or_b32 s23, s22, 0x14000
	v_mfma_f32_16x16x32_bf16 v[74:77], v[202:205], v[222:225], v[74:77]
	s_waitcnt lgkmcnt(6)
	v_mfma_f32_16x16x32_bf16 v[110:113], v[178:181], v[226:229], v[110:113]
	v_mfma_f32_16x16x32_bf16 v[102:105], v[194:197], v[226:229], v[102:105]
	v_mfma_f32_16x16x32_bf16 v[82:85], v[198:201], v[226:229], v[82:85]
	s_or_b32 s23, s22, 0x18000
	s_or_b32 s22, s22, 0x1c000
	v_mfma_f32_16x16x32_bf16 v[62:65], v[202:205], v[226:229], v[62:65]
	s_waitcnt lgkmcnt(5)
	v_mfma_f32_16x16x32_bf16 v[94:97], v[178:181], v[230:233], v[94:97]
	v_mfma_f32_16x16x32_bf16 v[86:89], v[194:197], v[230:233], v[86:89]
	v_mfma_f32_16x16x32_bf16 v[70:73], v[198:201], v[230:233], v[70:73]
	v_mfma_f32_16x16x32_bf16 v[54:57], v[202:205], v[230:233], v[54:57]
	s_waitcnt lgkmcnt(4)
	v_mfma_f32_16x16x32_bf16 v[78:81], v[178:181], v[234:237], v[78:81]
	v_mfma_f32_16x16x32_bf16 v[66:69], v[194:197], v[234:237], v[66:69]
	v_mfma_f32_16x16x32_bf16 v[58:61], v[198:201], v[234:237], v[58:61]
	v_mfma_f32_16x16x32_bf16 v[50:53], v[202:205], v[234:237], v[50:53]
	s_waitcnt lgkmcnt(0)
	s_barrier
	ds_read_b128 v[178:181], v182 offset:33792
	ds_read_b128 v[194:197], v182 offset:35840
	ds_read_b128 v[198:201], v182 offset:37888
	ds_read_b128 v[202:205], v182 offset:39936
	ds_read_b128 v[206:209], v238 offset:1024
	ds_read_b128 v[210:213], v238 offset:3072
	ds_read_b128 v[214:217], v238 offset:5120
	ds_read_b128 v[218:221], v238 offset:7168
	ds_read_b128 v[222:225], v238 offset:9216
	ds_read_b128 v[226:229], v238 offset:11264
	ds_read_b128 v[230:233], v238 offset:13312
	ds_read_b128 v[234:237], v238 offset:15360
	v_add_u32_e32 v182, s19, v190
	s_waitcnt vmcnt(3)
	ds_write_b128 v182, v[2:5] offset:32768
	s_waitcnt vmcnt(2)
	ds_write_b128 v182, v[6:9] offset:40960
	s_waitcnt vmcnt(1)
	ds_write_b128 v182, v[14:17] offset:49152
	s_waitcnt vmcnt(0)
	ds_write_b128 v182, v[26:29] offset:57344
	s_waitcnt lgkmcnt(0)
	s_barrier
	s_waitcnt lgkmcnt(11)
	v_mfma_f32_16x16x32_bf16 v[174:177], v[178:181], v[206:209], v[174:177]
	s_lshl_b32 s21, s21, 7
	s_and_b32 s21, s21, 0x780
	s_or_b32 s21, s21, s14
	s_or_b32 s22, s21, 0x20000
	v_mfma_f32_16x16x32_bf16 v[170:173], v[194:197], v[206:209], v[170:173]
	v_mfma_f32_16x16x32_bf16 v[158:161], v[198:201], v[206:209], v[158:161]
	v_mfma_f32_16x16x32_bf16 v[142:145], v[202:205], v[206:209], v[142:145]
	s_waitcnt lgkmcnt(10)
	v_mfma_f32_16x16x32_bf16 v[166:169], v[178:181], v[210:213], v[166:169]
	v_mfma_f32_16x16x32_bf16 v[162:165], v[194:197], v[210:213], v[162:165]
	v_mfma_f32_16x16x32_bf16 v[146:149], v[198:201], v[210:213], v[146:149]
	v_mfma_f32_16x16x32_bf16 v[122:125], v[202:205], v[210:213], v[122:125]
	s_waitcnt lgkmcnt(9)
	v_mfma_f32_16x16x32_bf16 v[154:157], v[178:181], v[214:217], v[154:157]
	v_mfma_f32_16x16x32_bf16 v[150:153], v[194:197], v[214:217], v[150:153]
	v_mfma_f32_16x16x32_bf16 v[130:133], v[198:201], v[214:217], v[130:133]
	v_mfma_f32_16x16x32_bf16 v[106:109], v[202:205], v[214:217], v[106:109]
	s_waitcnt lgkmcnt(8)
	v_mfma_f32_16x16x32_bf16 v[138:141], v[178:181], v[218:221], v[138:141]
	v_mfma_f32_16x16x32_bf16 v[134:137], v[194:197], v[218:221], v[134:137]
	s_or_b32 s22, s21, 0x40000
	s_or_b32 s21, s21, 0x60000
	v_mfma_f32_16x16x32_bf16 v[114:117], v[198:201], v[218:221], v[114:117]
	v_mfma_f32_16x16x32_bf16 v[90:93], v[202:205], v[218:221], v[90:93]
	s_waitcnt lgkmcnt(7)
	v_mfma_f32_16x16x32_bf16 v[126:129], v[178:181], v[222:225], v[126:129]
	v_mfma_f32_16x16x32_bf16 v[118:121], v[194:197], v[222:225], v[118:121]
	v_mfma_f32_16x16x32_bf16 v[98:101], v[198:201], v[222:225], v[98:101]
	v_mfma_f32_16x16x32_bf16 v[74:77], v[202:205], v[222:225], v[74:77]
	s_waitcnt lgkmcnt(6)
	v_mfma_f32_16x16x32_bf16 v[110:113], v[178:181], v[226:229], v[110:113]
	v_mfma_f32_16x16x32_bf16 v[102:105], v[194:197], v[226:229], v[102:105]
	v_mfma_f32_16x16x32_bf16 v[82:85], v[198:201], v[226:229], v[82:85]
	v_mfma_f32_16x16x32_bf16 v[62:65], v[202:205], v[226:229], v[62:65]
	s_waitcnt lgkmcnt(5)
	v_mfma_f32_16x16x32_bf16 v[94:97], v[178:181], v[230:233], v[94:97]
	v_mfma_f32_16x16x32_bf16 v[86:89], v[194:197], v[230:233], v[86:89]
	v_mfma_f32_16x16x32_bf16 v[70:73], v[198:201], v[230:233], v[70:73]
	v_mfma_f32_16x16x32_bf16 v[54:57], v[202:205], v[230:233], v[54:57]
	s_waitcnt lgkmcnt(4)
	v_mfma_f32_16x16x32_bf16 v[78:81], v[178:181], v[234:237], v[78:81]
	v_mfma_f32_16x16x32_bf16 v[66:69], v[194:197], v[234:237], v[66:69]
	v_mfma_f32_16x16x32_bf16 v[58:61], v[198:201], v[234:237], v[58:61]
	v_mfma_f32_16x16x32_bf16 v[50:53], v[202:205], v[234:237], v[50:53]
	s_waitcnt lgkmcnt(0)
	s_barrier
	s_add_i32 s20, s20, 1
	s_add_i32 s18, s18, 2
	v_add_u32_e32 v182, s19, v191
	v_add_u32_e32 v238, s19, v192
	ds_read_b128 v[178:181], v182 offset:32768
	ds_read_b128 v[194:197], v182 offset:34816
	ds_read_b128 v[198:201], v182 offset:36864
	ds_read_b128 v[202:205], v182 offset:38912
	ds_read_b128 v[206:209], v238
	ds_read_b128 v[210:213], v238 offset:2048
	ds_read_b128 v[214:217], v238 offset:4096
	ds_read_b128 v[218:221], v238 offset:6144
	ds_read_b128 v[222:225], v238 offset:8192
	ds_read_b128 v[226:229], v238 offset:10240
	ds_read_b128 v[230:233], v238 offset:12288
	ds_read_b128 v[234:237], v238 offset:14336
	s_min_u32 s21, s20, 29
	s_xor_b32 s19, s19, 0x10000
	v_add_u32_e32 v239, s19, v189
	s_waitcnt lgkmcnt(0)
	s_add_i32 s21, s21, 2
	s_barrier
	s_waitcnt lgkmcnt(11)
	v_mfma_f32_16x16x32_bf16 v[174:177], v[178:181], v[206:209], v[174:177]
	s_lshl_b32 s22, s21, 1
	s_and_b32 s22, s22, 0x60
	s_add_i32 s22, s22, s12
	s_lshl_b32 s22, s22, 6
	v_mfma_f32_16x16x32_bf16 v[170:173], v[194:197], v[206:209], v[170:173]
	s_and_b32 s22, s22, 0x3f00
	s_or_b32 s22, s22, s13
	s_lshl_b32 s23, s21, 23
	s_lshl_b32 s22, s22, 9
	v_mfma_f32_16x16x32_bf16 v[158:161], v[198:201], v[206:209], v[158:161]
	s_and_b32 s23, s23, 0x7000000
	s_or_b32 s22, s22, s23
	s_lshl_b32 s23, s21, 8
	s_and_b32 s23, s23, 0x100
	s_or_b32 s22, s22, s23
	s_or_b32 s23, s22, 0x4000
	v_mfma_f32_16x16x32_bf16 v[142:145], v[202:205], v[206:209], v[142:145]
	s_waitcnt lgkmcnt(10)
	v_mfma_f32_16x16x32_bf16 v[166:169], v[178:181], v[210:213], v[166:169]
	v_mfma_f32_16x16x32_bf16 v[162:165], v[194:197], v[210:213], v[162:165]
	v_mfma_f32_16x16x32_bf16 v[146:149], v[198:201], v[210:213], v[146:149]
	s_or_b32 s23, s22, 0x8000
	v_mfma_f32_16x16x32_bf16 v[122:125], v[202:205], v[210:213], v[122:125]
	s_waitcnt lgkmcnt(9)
	v_mfma_f32_16x16x32_bf16 v[154:157], v[178:181], v[214:217], v[154:157]
	v_mfma_f32_16x16x32_bf16 v[150:153], v[194:197], v[214:217], v[150:153]
	v_mfma_f32_16x16x32_bf16 v[130:133], v[198:201], v[214:217], v[130:133]
	s_or_b32 s23, s22, 0xc000
	v_mfma_f32_16x16x32_bf16 v[106:109], v[202:205], v[214:217], v[106:109]
	s_waitcnt lgkmcnt(8)
	v_mfma_f32_16x16x32_bf16 v[138:141], v[178:181], v[218:221], v[138:141]
	v_mfma_f32_16x16x32_bf16 v[134:137], v[194:197], v[218:221], v[134:137]
	v_mfma_f32_16x16x32_bf16 v[114:117], v[198:201], v[218:221], v[114:117]
	s_or_b32 s23, s22, 0x10000
	v_mfma_f32_16x16x32_bf16 v[90:93], v[202:205], v[218:221], v[90:93]
	s_waitcnt lgkmcnt(7)
	v_mfma_f32_16x16x32_bf16 v[126:129], v[178:181], v[222:225], v[126:129]
	v_mfma_f32_16x16x32_bf16 v[118:121], v[194:197], v[222:225], v[118:121]
	v_mfma_f32_16x16x32_bf16 v[98:101], v[198:201], v[222:225], v[98:101]
	s_or_b32 s23, s22, 0x14000
	v_mfma_f32_16x16x32_bf16 v[74:77], v[202:205], v[222:225], v[74:77]
	s_waitcnt lgkmcnt(6)
	v_mfma_f32_16x16x32_bf16 v[110:113], v[178:181], v[226:229], v[110:113]
	v_mfma_f32_16x16x32_bf16 v[102:105], v[194:197], v[226:229], v[102:105]
	v_mfma_f32_16x16x32_bf16 v[82:85], v[198:201], v[226:229], v[82:85]
	s_or_b32 s23, s22, 0x18000
	s_or_b32 s22, s22, 0x1c000
	v_mfma_f32_16x16x32_bf16 v[62:65], v[202:205], v[226:229], v[62:65]
	s_waitcnt lgkmcnt(5)
	v_mfma_f32_16x16x32_bf16 v[94:97], v[178:181], v[230:233], v[94:97]
	v_mfma_f32_16x16x32_bf16 v[86:89], v[194:197], v[230:233], v[86:89]
	v_mfma_f32_16x16x32_bf16 v[70:73], v[198:201], v[230:233], v[70:73]
	v_mfma_f32_16x16x32_bf16 v[54:57], v[202:205], v[230:233], v[54:57]
	s_waitcnt lgkmcnt(4)
	v_mfma_f32_16x16x32_bf16 v[78:81], v[178:181], v[234:237], v[78:81]
	v_mfma_f32_16x16x32_bf16 v[66:69], v[194:197], v[234:237], v[66:69]
	v_mfma_f32_16x16x32_bf16 v[58:61], v[198:201], v[234:237], v[58:61]
	v_mfma_f32_16x16x32_bf16 v[50:53], v[202:205], v[234:237], v[50:53]
	s_waitcnt lgkmcnt(0)
	s_barrier
	ds_read_b128 v[178:181], v182 offset:33792
	ds_read_b128 v[194:197], v182 offset:35840
	ds_read_b128 v[198:201], v182 offset:37888
	ds_read_b128 v[202:205], v182 offset:39936
	ds_read_b128 v[206:209], v238 offset:1024
	ds_read_b128 v[210:213], v238 offset:3072
	ds_read_b128 v[214:217], v238 offset:5120
	ds_read_b128 v[218:221], v238 offset:7168
	ds_read_b128 v[222:225], v238 offset:9216
	ds_read_b128 v[226:229], v238 offset:11264
	ds_read_b128 v[230:233], v238 offset:13312
	ds_read_b128 v[234:237], v238 offset:15360
	s_waitcnt lgkmcnt(0)
	s_barrier
	s_waitcnt lgkmcnt(11)
	v_mfma_f32_16x16x32_bf16 v[174:177], v[178:181], v[206:209], v[174:177]
	s_lshl_b32 s21, s21, 7
	s_and_b32 s21, s21, 0x780
	s_or_b32 s21, s21, s14
	s_or_b32 s22, s21, 0x20000
	v_mfma_f32_16x16x32_bf16 v[170:173], v[194:197], v[206:209], v[170:173]
	v_mfma_f32_16x16x32_bf16 v[158:161], v[198:201], v[206:209], v[158:161]
	v_mfma_f32_16x16x32_bf16 v[142:145], v[202:205], v[206:209], v[142:145]
	s_waitcnt lgkmcnt(10)
	v_mfma_f32_16x16x32_bf16 v[166:169], v[178:181], v[210:213], v[166:169]
	v_mfma_f32_16x16x32_bf16 v[162:165], v[194:197], v[210:213], v[162:165]
	v_mfma_f32_16x16x32_bf16 v[146:149], v[198:201], v[210:213], v[146:149]
	v_mfma_f32_16x16x32_bf16 v[122:125], v[202:205], v[210:213], v[122:125]
	s_waitcnt lgkmcnt(9)
	v_mfma_f32_16x16x32_bf16 v[154:157], v[178:181], v[214:217], v[154:157]
	v_mfma_f32_16x16x32_bf16 v[150:153], v[194:197], v[214:217], v[150:153]
	v_mfma_f32_16x16x32_bf16 v[130:133], v[198:201], v[214:217], v[130:133]
	v_mfma_f32_16x16x32_bf16 v[106:109], v[202:205], v[214:217], v[106:109]
	s_waitcnt lgkmcnt(8)
	v_mfma_f32_16x16x32_bf16 v[138:141], v[178:181], v[218:221], v[138:141]
	v_mfma_f32_16x16x32_bf16 v[134:137], v[194:197], v[218:221], v[134:137]
	s_or_b32 s22, s21, 0x40000
	s_or_b32 s21, s21, 0x60000
	v_mfma_f32_16x16x32_bf16 v[114:117], v[198:201], v[218:221], v[114:117]
	v_mfma_f32_16x16x32_bf16 v[90:93], v[202:205], v[218:221], v[90:93]
	s_waitcnt lgkmcnt(7)
	v_mfma_f32_16x16x32_bf16 v[126:129], v[178:181], v[222:225], v[126:129]
	v_mfma_f32_16x16x32_bf16 v[118:121], v[194:197], v[222:225], v[118:121]
	v_mfma_f32_16x16x32_bf16 v[98:101], v[198:201], v[222:225], v[98:101]
	v_mfma_f32_16x16x32_bf16 v[74:77], v[202:205], v[222:225], v[74:77]
	s_waitcnt lgkmcnt(6)
	v_mfma_f32_16x16x32_bf16 v[110:113], v[178:181], v[226:229], v[110:113]
	v_mfma_f32_16x16x32_bf16 v[102:105], v[194:197], v[226:229], v[102:105]
	v_mfma_f32_16x16x32_bf16 v[82:85], v[198:201], v[226:229], v[82:85]
	v_mfma_f32_16x16x32_bf16 v[62:65], v[202:205], v[226:229], v[62:65]
	s_waitcnt lgkmcnt(5)
	v_mfma_f32_16x16x32_bf16 v[94:97], v[178:181], v[230:233], v[94:97]
	v_mfma_f32_16x16x32_bf16 v[86:89], v[194:197], v[230:233], v[86:89]
	v_mfma_f32_16x16x32_bf16 v[70:73], v[198:201], v[230:233], v[70:73]
	v_mfma_f32_16x16x32_bf16 v[54:57], v[202:205], v[230:233], v[54:57]
	s_waitcnt lgkmcnt(4)
	v_mfma_f32_16x16x32_bf16 v[78:81], v[178:181], v[234:237], v[78:81]
	v_mfma_f32_16x16x32_bf16 v[66:69], v[194:197], v[234:237], v[66:69]
	v_mfma_f32_16x16x32_bf16 v[58:61], v[198:201], v[234:237], v[58:61]
	v_mfma_f32_16x16x32_bf16 v[50:53], v[202:205], v[234:237], v[50:53]
	s_and_b32 s21, s18, 32
	s_add_i32 s21, s21, s12
	s_lshl_b32 s21, s21, 6
	s_and_b32 s21, s21, 0x3f00
	v_add_lshl_u32 v182, v193, s21, 9
	v_lshl_add_u64 v[206:207], v[184:185], 0, v[182:183]
	v_add_co_u32_e32 v208, vcc, s8, v206
	s_nop 1
	v_addc_co_u32_e32 v209, vcc, 0, v207, vcc
	v_add_co_u32_e32 v210, vcc, s15, v206
	s_nop 1
	v_addc_co_u32_e32 v211, vcc, 0, v207, vcc
	v_add_co_u32_e32 v212, vcc, s9, v206
	s_nop 1
	v_addc_co_u32_e32 v213, vcc, 0, v207, vcc
	v_add_co_u32_e32 v214, vcc, s16, v206
	s_nop 1
	v_addc_co_u32_e32 v215, vcc, 0, v207, vcc
	v_add_co_u32_e32 v216, vcc, s10, v206
	s_nop 1
	v_addc_co_u32_e32 v217, vcc, 0, v207, vcc
	v_add_co_u32_e32 v218, vcc, s17, v206
	s_nop 1
	v_addc_co_u32_e32 v219, vcc, 0, v207, vcc
	v_add_co_u32_e32 v220, vcc, s11, v206
	s_nop 1
	v_addc_co_u32_e32 v221, vcc, 0, v207, vcc
	global_store_dwordx4 v[206:207], v[174:177], off
	global_store_dwordx4 v[206:207], v[170:173], off offset:64
	global_store_dwordx4 v[206:207], v[158:161], off offset:128
	global_store_dwordx4 v[206:207], v[142:145], off offset:192
	global_store_dwordx4 v[208:209], v[166:169], off
	global_store_dwordx4 v[208:209], v[162:165], off offset:64
	global_store_dwordx4 v[208:209], v[146:149], off offset:128
	global_store_dwordx4 v[208:209], v[122:125], off offset:192
	global_store_dwordx4 v[210:211], v[154:157], off
	global_store_dwordx4 v[210:211], v[150:153], off offset:64
	global_store_dwordx4 v[210:211], v[130:133], off offset:128
	global_store_dwordx4 v[210:211], v[106:109], off offset:192
	global_store_dwordx4 v[212:213], v[138:141], off
	global_store_dwordx4 v[212:213], v[134:137], off offset:64
	global_store_dwordx4 v[212:213], v[114:117], off offset:128
	global_store_dwordx4 v[212:213], v[90:93], off offset:192
	global_store_dwordx4 v[214:215], v[126:129], off
	global_store_dwordx4 v[214:215], v[118:121], off offset:64
	global_store_dwordx4 v[214:215], v[98:101], off offset:128
	global_store_dwordx4 v[214:215], v[74:77], off offset:192
	global_store_dwordx4 v[216:217], v[110:113], off
	global_store_dwordx4 v[216:217], v[102:105], off offset:64
	global_store_dwordx4 v[216:217], v[82:85], off offset:128
	global_store_dwordx4 v[216:217], v[62:65], off offset:192
	global_store_dwordx4 v[218:219], v[94:97], off
	global_store_dwordx4 v[218:219], v[86:89], off offset:64
	global_store_dwordx4 v[218:219], v[70:73], off offset:128
	global_store_dwordx4 v[218:219], v[54:57], off offset:192
	global_store_dwordx4 v[220:221], v[78:81], off
	global_store_dwordx4 v[220:221], v[66:69], off offset:64
	global_store_dwordx4 v[220:221], v[58:61], off offset:128
	global_store_dwordx4 v[220:221], v[50:53], off offset:192
	s_waitcnt lgkmcnt(0)
	s_barrier
	s_branch .LBB1_6
.Lfirst:
	v_add_u32_e32 v182, s19, v191
	v_add_u32_e32 v238, s19, v192
	ds_read_b128 v[178:181], v182 offset:32768
	ds_read_b128 v[194:197], v182 offset:34816
	ds_read_b128 v[198:201], v182 offset:36864
	ds_read_b128 v[202:205], v182 offset:38912
	ds_read_b128 v[206:209], v238
	ds_read_b128 v[210:213], v238 offset:2048
	ds_read_b128 v[214:217], v238 offset:4096
	ds_read_b128 v[218:221], v238 offset:6144
	ds_read_b128 v[222:225], v238 offset:8192
	ds_read_b128 v[226:229], v238 offset:10240
	ds_read_b128 v[230:233], v238 offset:12288
	ds_read_b128 v[234:237], v238 offset:14336
	s_min_u32 s21, s20, 29
	s_xor_b32 s19, s19, 0x10000
	v_add_u32_e32 v239, s19, v189
	s_waitcnt vmcnt(11)
	v_cvt_pk_bf16_f32 v13, v12, v13
	v_cvt_pk_bf16_f32 v12, v10, v11
	s_waitcnt vmcnt(10)
	v_cvt_pk_bf16_f32 v11, v20, v21
	v_cvt_pk_bf16_f32 v10, v18, v19
	ds_write2st64_b64 v239, v[12:13], v[10:11] offset1:8
	s_waitcnt vmcnt(9)
	v_cvt_pk_bf16_f32 v11, v24, v25
	v_cvt_pk_bf16_f32 v10, v22, v23
	s_waitcnt vmcnt(8)
	v_cvt_pk_bf16_f32 v13, v32, v33
	v_cvt_pk_bf16_f32 v12, v30, v31
	ds_write2st64_b64 v239, v[10:11], v[12:13] offset0:16 offset1:24
	s_waitcnt vmcnt(7)
	v_cvt_pk_bf16_f32 v11, v36, v37
	v_cvt_pk_bf16_f32 v10, v34, v35
	s_waitcnt vmcnt(6)
	v_cvt_pk_bf16_f32 v13, v40, v41
	v_cvt_pk_bf16_f32 v12, v38, v39
	ds_write2st64_b64 v239, v[10:11], v[12:13] offset0:32 offset1:40
	s_waitcnt vmcnt(5)
	v_cvt_pk_bf16_f32 v11, v44, v45
	v_cvt_pk_bf16_f32 v10, v42, v43
	s_waitcnt vmcnt(4)
	v_cvt_pk_bf16_f32 v13, v48, v49
	v_cvt_pk_bf16_f32 v12, v46, v47
	ds_write2st64_b64 v239, v[10:11], v[12:13] offset0:48 offset1:56
	s_waitcnt lgkmcnt(0)
	s_add_i32 s21, s21, 2
	s_barrier
	s_waitcnt lgkmcnt(11)
	v_mfma_f32_16x16x32_bf16 v[174:177], v[178:181], v[206:209], v[240:243]
	s_lshl_b32 s22, s21, 1
	s_and_b32 s22, s22, 0x60
	s_add_i32 s22, s22, s12
	s_lshl_b32 s22, s22, 6
	v_mfma_f32_16x16x32_bf16 v[170:173], v[194:197], v[206:209], v[244:247]
	s_and_b32 s22, s22, 0x3f00
	s_or_b32 s22, s22, s13
	s_lshl_b32 s23, s21, 23
	s_lshl_b32 s22, s22, 9
	v_mfma_f32_16x16x32_bf16 v[158:161], v[198:201], v[206:209], v[248:251]
	s_and_b32 s23, s23, 0x7000000
	s_or_b32 s22, s22, s23
	s_lshl_b32 s23, s21, 8
	s_and_b32 s23, s23, 0x100
	s_or_b32 s22, s22, s23
	s_or_b32 s23, s22, 0x4000
	buffer_load_dwordx4 v[10:13], v1, s[4:7], s22 offen sc0 nt
	v_mfma_f32_16x16x32_bf16 v[142:145], v[202:205], v[206:209], v[252:255]
	s_waitcnt lgkmcnt(10)
	v_mfma_f32_16x16x32_bf16 v[166:169], v[178:181], v[210:213], v[240:243]
	v_mfma_f32_16x16x32_bf16 v[162:165], v[194:197], v[210:213], v[244:247]
	v_mfma_f32_16x16x32_bf16 v[146:149], v[198:201], v[210:213], v[248:251]
	buffer_load_dwordx4 v[18:21], v1, s[4:7], s23 offen sc0 nt
	s_or_b32 s23, s22, 0x8000
	v_mfma_f32_16x16x32_bf16 v[122:125], v[202:205], v[210:213], v[252:255]
	s_waitcnt lgkmcnt(9)
	v_mfma_f32_16x16x32_bf16 v[154:157], v[178:181], v[214:217], v[240:243]
	v_mfma_f32_16x16x32_bf16 v[150:153], v[194:197], v[214:217], v[244:247]
	v_mfma_f32_16x16x32_bf16 v[130:133], v[198:201], v[214:217], v[248:251]
	buffer_load_dwordx4 v[22:25], v1, s[4:7], s23 offen sc0 nt
	s_or_b32 s23, s22, 0xc000
	v_mfma_f32_16x16x32_bf16 v[106:109], v[202:205], v[214:217], v[252:255]
	s_waitcnt lgkmcnt(8)
	v_mfma_f32_16x16x32_bf16 v[138:141], v[178:181], v[218:221], v[240:243]
	v_mfma_f32_16x16x32_bf16 v[134:137], v[194:197], v[218:221], v[244:247]
	v_mfma_f32_16x16x32_bf16 v[114:117], v[198:201], v[218:221], v[248:251]
	buffer_load_dwordx4 v[30:33], v1, s[4:7], s23 offen sc0 nt
	s_or_b32 s23, s22, 0x10000
	v_mfma_f32_16x16x32_bf16 v[90:93], v[202:205], v[218:221], v[252:255]
	s_waitcnt lgkmcnt(7)
	v_mfma_f32_16x16x32_bf16 v[126:129], v[178:181], v[222:225], v[240:243]
	v_mfma_f32_16x16x32_bf16 v[118:121], v[194:197], v[222:225], v[244:247]
	v_mfma_f32_16x16x32_bf16 v[98:101], v[198:201], v[222:225], v[248:251]
	buffer_load_dwordx4 v[34:37], v1, s[4:7], s23 offen sc0 nt
	s_or_b32 s23, s22, 0x14000
	v_mfma_f32_16x16x32_bf16 v[74:77], v[202:205], v[222:225], v[252:255]
	s_waitcnt lgkmcnt(6)
	v_mfma_f32_16x16x32_bf16 v[110:113], v[178:181], v[226:229], v[240:243]
	v_mfma_f32_16x16x32_bf16 v[102:105], v[194:197], v[226:229], v[244:247]
	v_mfma_f32_16x16x32_bf16 v[82:85], v[198:201], v[226:229], v[248:251]
	buffer_load_dwordx4 v[38:41], v1, s[4:7], s23 offen sc0 nt
	s_or_b32 s23, s22, 0x18000
	s_or_b32 s22, s22, 0x1c000
	v_mfma_f32_16x16x32_bf16 v[62:65], v[202:205], v[226:229], v[252:255]
	s_waitcnt lgkmcnt(5)
	v_mfma_f32_16x16x32_bf16 v[94:97], v[178:181], v[230:233], v[240:243]
	v_mfma_f32_16x16x32_bf16 v[86:89], v[194:197], v[230:233], v[244:247]
	v_mfma_f32_16x16x32_bf16 v[70:73], v[198:201], v[230:233], v[248:251]
	buffer_load_dwordx4 v[42:45], v1, s[4:7], s23 offen sc0 nt
	v_mfma_f32_16x16x32_bf16 v[54:57], v[202:205], v[230:233], v[252:255]
	s_waitcnt lgkmcnt(4)
	v_mfma_f32_16x16x32_bf16 v[78:81], v[178:181], v[234:237], v[240:243]
	v_mfma_f32_16x16x32_bf16 v[66:69], v[194:197], v[234:237], v[244:247]
	v_mfma_f32_16x16x32_bf16 v[58:61], v[198:201], v[234:237], v[248:251]
	buffer_load_dwordx4 v[46:49], v1, s[4:7], s22 offen sc0 nt
	v_mfma_f32_16x16x32_bf16 v[50:53], v[202:205], v[234:237], v[252:255]
	s_waitcnt lgkmcnt(0)
	s_barrier
	ds_read_b128 v[178:181], v182 offset:33792
	ds_read_b128 v[194:197], v182 offset:35840
	ds_read_b128 v[198:201], v182 offset:37888
	ds_read_b128 v[202:205], v182 offset:39936
	ds_read_b128 v[206:209], v238 offset:1024
	ds_read_b128 v[210:213], v238 offset:3072
	ds_read_b128 v[214:217], v238 offset:5120
	ds_read_b128 v[218:221], v238 offset:7168
	ds_read_b128 v[222:225], v238 offset:9216
	ds_read_b128 v[226:229], v238 offset:11264
	ds_read_b128 v[230:233], v238 offset:13312
	ds_read_b128 v[234:237], v238 offset:15360
	v_add_u32_e32 v182, s19, v190
	s_waitcnt vmcnt(11)
	ds_write_b128 v182, v[2:5] offset:32768
	s_waitcnt vmcnt(10)
	ds_write_b128 v182, v[6:9] offset:40960
	s_waitcnt vmcnt(9)
	ds_write_b128 v182, v[14:17] offset:49152
	s_waitcnt vmcnt(8)
	ds_write_b128 v182, v[26:29] offset:57344
	s_waitcnt lgkmcnt(0)
	s_barrier
	s_waitcnt lgkmcnt(11)
	v_mfma_f32_16x16x32_bf16 v[174:177], v[178:181], v[206:209], v[174:177]
	s_lshl_b32 s21, s21, 7
	s_and_b32 s21, s21, 0x780
	s_or_b32 s21, s21, s14
	s_or_b32 s22, s21, 0x20000
	v_mfma_f32_16x16x32_bf16 v[170:173], v[194:197], v[206:209], v[170:173]
	v_mfma_f32_16x16x32_bf16 v[158:161], v[198:201], v[206:209], v[158:161]
	v_mfma_f32_16x16x32_bf16 v[142:145], v[202:205], v[206:209], v[142:145]
	s_waitcnt lgkmcnt(10)
	v_mfma_f32_16x16x32_bf16 v[166:169], v[178:181], v[210:213], v[166:169]
	v_mfma_f32_16x16x32_bf16 v[162:165], v[194:197], v[210:213], v[162:165]
	buffer_load_dwordx4 v[2:5], v188, s[0:3], s21 offen sc1
	v_mfma_f32_16x16x32_bf16 v[146:149], v[198:201], v[210:213], v[146:149]
	v_mfma_f32_16x16x32_bf16 v[122:125], v[202:205], v[210:213], v[122:125]
	s_waitcnt lgkmcnt(9)
	v_mfma_f32_16x16x32_bf16 v[154:157], v[178:181], v[214:217], v[154:157]
	v_mfma_f32_16x16x32_bf16 v[150:153], v[194:197], v[214:217], v[150:153]
	v_mfma_f32_16x16x32_bf16 v[130:133], v[198:201], v[214:217], v[130:133]
	v_mfma_f32_16x16x32_bf16 v[106:109], v[202:205], v[214:217], v[106:109]
	s_waitcnt lgkmcnt(8)
	v_mfma_f32_16x16x32_bf16 v[138:141], v[178:181], v[218:221], v[138:141]
	v_mfma_f32_16x16x32_bf16 v[134:137], v[194:197], v[218:221], v[134:137]
	buffer_load_dwordx4 v[6:9], v188, s[0:3], s22 offen sc1
	s_or_b32 s22, s21, 0x40000
	s_or_b32 s21, s21, 0x60000
	v_mfma_f32_16x16x32_bf16 v[114:117], v[198:201], v[218:221], v[114:117]
	v_mfma_f32_16x16x32_bf16 v[90:93], v[202:205], v[218:221], v[90:93]
	s_waitcnt lgkmcnt(7)
	v_mfma_f32_16x16x32_bf16 v[126:129], v[178:181], v[222:225], v[126:129]
	v_mfma_f32_16x16x32_bf16 v[118:121], v[194:197], v[222:225], v[118:121]
	v_mfma_f32_16x16x32_bf16 v[98:101], v[198:201], v[222:225], v[98:101]
	v_mfma_f32_16x16x32_bf16 v[74:77], v[202:205], v[222:225], v[74:77]
	s_waitcnt lgkmcnt(6)
	v_mfma_f32_16x16x32_bf16 v[110:113], v[178:181], v[226:229], v[110:113]
	v_mfma_f32_16x16x32_bf16 v[102:105], v[194:197], v[226:229], v[102:105]
	buffer_load_dwordx4 v[14:17], v188, s[0:3], s22 offen sc1
	v_mfma_f32_16x16x32_bf16 v[82:85], v[198:201], v[226:229], v[82:85]
	v_mfma_f32_16x16x32_bf16 v[62:65], v[202:205], v[226:229], v[62:65]
	s_waitcnt lgkmcnt(5)
	v_mfma_f32_16x16x32_bf16 v[94:97], v[178:181], v[230:233], v[94:97]
	v_mfma_f32_16x16x32_bf16 v[86:89], v[194:197], v[230:233], v[86:89]
	v_mfma_f32_16x16x32_bf16 v[70:73], v[198:201], v[230:233], v[70:73]
	v_mfma_f32_16x16x32_bf16 v[54:57], v[202:205], v[230:233], v[54:57]
	s_waitcnt lgkmcnt(4)
	v_mfma_f32_16x16x32_bf16 v[78:81], v[178:181], v[234:237], v[78:81]
	v_mfma_f32_16x16x32_bf16 v[66:69], v[194:197], v[234:237], v[66:69]
	buffer_load_dwordx4 v[26:29], v188, s[0:3], s21 offen sc1
	v_mfma_f32_16x16x32_bf16 v[58:61], v[198:201], v[234:237], v[58:61]
	v_mfma_f32_16x16x32_bf16 v[50:53], v[202:205], v[234:237], v[50:53]
	s_branch .LBB1_3
